# moe_tables in P7: 16 count loads per thread in flight, expert starts + tile->expert table computed by all threads in parallel (was one thread serial)
# speedup vs baseline: 1.0248x; 1.0072x over previous
.LBB0_1083:
	s_cmp_le_i32 s90, s14
	s_cselect_b64 s[4:5], -1, 0
	s_and_b64 s[0:1], s[4:5], s[0:1]
	s_xor_b64 s[8:9], s[0:1], -1
	s_and_b64 vcc, exec, s[8:9]
	s_cbranch_vccnz .LBB0_1136
	s_mov_b64 s[0:1], s[84:85]
	s_load_dwordx2 s[6:7], s[0:1], 0x100
	s_mov_b32 s0, s86
	v_mov_b32_e32 v3, 0
	v_lshl_add_u32 v8, s0, 6, v213
	v_mov_b32_e32 v6, 0
	v_ashrrev_i32_e32 v2, 5, v8
	v_and_b32_e32 v0, 31, v8
	v_cmp_gt_i32_e32 vcc, s83, v2
	s_and_saveexec_b64 s[10:11], vcc
	v_readlane_b32 s14, v253, 53
	s_cbranch_execz .LBB0_1096
	s_waitcnt lgkmcnt(0)
	s_add_u32 s12, s6, 0x23c000
	s_addc_u32 s13, s7, 0
	v_lshlrev_b32_e32 v4, 2, v8
	global_load_dword v20, v4, s[12:13]
	global_load_dword v21, v4, s[12:13] offset:2048
	s_add_u32 s12, s12, 0x1000
	s_addc_u32 s13, s13, 0
	global_load_dword v22, v4, s[12:13]
	global_load_dword v23, v4, s[12:13] offset:2048
	s_add_u32 s12, s12, 0x1000
	s_addc_u32 s13, s13, 0
	global_load_dword v24, v4, s[12:13]
	global_load_dword v25, v4, s[12:13] offset:2048
	s_add_u32 s12, s12, 0x1000
	s_addc_u32 s13, s13, 0
	global_load_dword v26, v4, s[12:13]
	global_load_dword v27, v4, s[12:13] offset:2048
	s_add_u32 s12, s12, 0x1000
	s_addc_u32 s13, s13, 0
	global_load_dword v28, v4, s[12:13]
	global_load_dword v29, v4, s[12:13] offset:2048
	s_add_u32 s12, s12, 0x1000
	s_addc_u32 s13, s13, 0
	global_load_dword v30, v4, s[12:13]
	global_load_dword v31, v4, s[12:13] offset:2048
	s_add_u32 s12, s12, 0x1000
	s_addc_u32 s13, s13, 0
	global_load_dword v32, v4, s[12:13]
	global_load_dword v33, v4, s[12:13] offset:2048
	s_add_u32 s12, s12, 0x1000
	s_addc_u32 s13, s13, 0
	global_load_dword v34, v4, s[12:13]
	global_load_dword v35, v4, s[12:13] offset:2048
	v_mov_b32_e32 v6, 0
	v_mov_b32_e32 v3, 0
	s_waitcnt vmcnt(15)
	v_mov_b32_e32 v5, v2
	v_cmp_gt_i32_e32 vcc, s83, v5
	v_cndmask_b32_e32 v7, 0, v20, vcc
	v_add_u32_e32 v6, v6, v7
	v_cmp_gt_i32_e32 vcc, s82, v5
	v_cndmask_b32_e32 v7, 0, v7, vcc
	v_add_u32_e32 v3, v3, v7
	s_waitcnt vmcnt(14)
	v_add_u32_e32 v5, 16, v2
	v_cmp_gt_i32_e32 vcc, s83, v5
	v_cndmask_b32_e32 v7, 0, v21, vcc
	v_add_u32_e32 v6, v6, v7
	v_cmp_gt_i32_e32 vcc, s82, v5
	v_cndmask_b32_e32 v7, 0, v7, vcc
	v_add_u32_e32 v3, v3, v7
	s_waitcnt vmcnt(13)
	v_add_u32_e32 v5, 32, v2
	v_cmp_gt_i32_e32 vcc, s83, v5
	v_cndmask_b32_e32 v7, 0, v22, vcc
	v_add_u32_e32 v6, v6, v7
	v_cmp_gt_i32_e32 vcc, s82, v5
	v_cndmask_b32_e32 v7, 0, v7, vcc
	v_add_u32_e32 v3, v3, v7
	s_waitcnt vmcnt(12)
	v_add_u32_e32 v5, 48, v2
	v_cmp_gt_i32_e32 vcc, s83, v5
	v_cndmask_b32_e32 v7, 0, v23, vcc
	v_add_u32_e32 v6, v6, v7
	v_cmp_gt_i32_e32 vcc, s82, v5
	v_cndmask_b32_e32 v7, 0, v7, vcc
	v_add_u32_e32 v3, v3, v7
	s_waitcnt vmcnt(11)
	v_add_u32_e32 v5, 64, v2
	v_cmp_gt_i32_e32 vcc, s83, v5
	v_cndmask_b32_e32 v7, 0, v24, vcc
	v_add_u32_e32 v6, v6, v7
	v_cmp_gt_i32_e32 vcc, s82, v5
	v_cndmask_b32_e32 v7, 0, v7, vcc
	v_add_u32_e32 v3, v3, v7
	s_waitcnt vmcnt(10)
	v_add_u32_e32 v5, 0x50, v2
	v_cmp_gt_i32_e32 vcc, s83, v5
	v_cndmask_b32_e32 v7, 0, v25, vcc
	v_add_u32_e32 v6, v6, v7
	v_cmp_gt_i32_e32 vcc, s82, v5
	v_cndmask_b32_e32 v7, 0, v7, vcc
	v_add_u32_e32 v3, v3, v7
	s_waitcnt vmcnt(9)
	v_add_u32_e32 v5, 0x60, v2
	v_cmp_gt_i32_e32 vcc, s83, v5
	v_cndmask_b32_e32 v7, 0, v26, vcc
	v_add_u32_e32 v6, v6, v7
	v_cmp_gt_i32_e32 vcc, s82, v5
	v_cndmask_b32_e32 v7, 0, v7, vcc
	v_add_u32_e32 v3, v3, v7
	s_waitcnt vmcnt(8)
	v_add_u32_e32 v5, 0x70, v2
	v_cmp_gt_i32_e32 vcc, s83, v5
	v_cndmask_b32_e32 v7, 0, v27, vcc
	v_add_u32_e32 v6, v6, v7
	v_cmp_gt_i32_e32 vcc, s82, v5
	v_cndmask_b32_e32 v7, 0, v7, vcc
	v_add_u32_e32 v3, v3, v7
	s_waitcnt vmcnt(7)
	v_add_u32_e32 v5, 0x80, v2
	v_cmp_gt_i32_e32 vcc, s83, v5
	v_cndmask_b32_e32 v7, 0, v28, vcc
	v_add_u32_e32 v6, v6, v7
	v_cmp_gt_i32_e32 vcc, s82, v5
	v_cndmask_b32_e32 v7, 0, v7, vcc
	v_add_u32_e32 v3, v3, v7
	s_waitcnt vmcnt(6)
	v_add_u32_e32 v5, 0x90, v2
	v_cmp_gt_i32_e32 vcc, s83, v5
	v_cndmask_b32_e32 v7, 0, v29, vcc
	v_add_u32_e32 v6, v6, v7
	v_cmp_gt_i32_e32 vcc, s82, v5
	v_cndmask_b32_e32 v7, 0, v7, vcc
	v_add_u32_e32 v3, v3, v7
	s_waitcnt vmcnt(5)
	v_add_u32_e32 v5, 0xa0, v2
	v_cmp_gt_i32_e32 vcc, s83, v5
	v_cndmask_b32_e32 v7, 0, v30, vcc
	v_add_u32_e32 v6, v6, v7
	v_cmp_gt_i32_e32 vcc, s82, v5
	v_cndmask_b32_e32 v7, 0, v7, vcc
	v_add_u32_e32 v3, v3, v7
	s_waitcnt vmcnt(4)
	v_add_u32_e32 v5, 0xb0, v2
	v_cmp_gt_i32_e32 vcc, s83, v5
	v_cndmask_b32_e32 v7, 0, v31, vcc
	v_add_u32_e32 v6, v6, v7
	v_cmp_gt_i32_e32 vcc, s82, v5
	v_cndmask_b32_e32 v7, 0, v7, vcc
	v_add_u32_e32 v3, v3, v7
	s_waitcnt vmcnt(3)
	v_add_u32_e32 v5, 0xc0, v2
	v_cmp_gt_i32_e32 vcc, s83, v5
	v_cndmask_b32_e32 v7, 0, v32, vcc
	v_add_u32_e32 v6, v6, v7
	v_cmp_gt_i32_e32 vcc, s82, v5
	v_cndmask_b32_e32 v7, 0, v7, vcc
	v_add_u32_e32 v3, v3, v7
	s_waitcnt vmcnt(2)
	v_add_u32_e32 v5, 0xd0, v2
	v_cmp_gt_i32_e32 vcc, s83, v5
	v_cndmask_b32_e32 v7, 0, v33, vcc
	v_add_u32_e32 v6, v6, v7
	v_cmp_gt_i32_e32 vcc, s82, v5
	v_cndmask_b32_e32 v7, 0, v7, vcc
	v_add_u32_e32 v3, v3, v7
	s_waitcnt vmcnt(1)
	v_add_u32_e32 v5, 0xe0, v2
	v_cmp_gt_i32_e32 vcc, s83, v5
	v_cndmask_b32_e32 v7, 0, v34, vcc
	v_add_u32_e32 v6, v6, v7
	v_cmp_gt_i32_e32 vcc, s82, v5
	v_cndmask_b32_e32 v7, 0, v7, vcc
	v_add_u32_e32 v3, v3, v7
	s_waitcnt vmcnt(0)
	v_add_u32_e32 v5, 0xf0, v2
	v_cmp_gt_i32_e32 vcc, s83, v5
	v_cndmask_b32_e32 v7, 0, v35, vcc
	v_add_u32_e32 v6, v6, v7
	v_cmp_gt_i32_e32 vcc, s82, v5
	v_cndmask_b32_e32 v7, 0, v7, vcc
	v_add_u32_e32 v3, v3, v7

.LBB0_1098:
	s_or_b64 exec, exec, s[0:1]
	s_waitcnt lgkmcnt(0)
	s_barrier
	v_mov_b32_e32 v2, 0x1000
	ds_read_b128 v[20:23], v2
	ds_read_b128 v[24:27], v2 offset:16
	ds_read_b128 v[28:31], v2 offset:32
	ds_read_b128 v[32:35], v2 offset:48
	ds_read_b128 v[36:39], v2 offset:64
	ds_read_b128 v[40:43], v2 offset:80
	ds_read_b128 v[44:47], v2 offset:96
	ds_read_b128 v[48:51], v2 offset:112
	s_waitcnt lgkmcnt(0)
	v_add_u32_e32 v21, v21, v20
	v_add_u32_e32 v22, v22, v21
	v_add_u32_e32 v23, v23, v22
	v_add_u32_e32 v24, v24, v23
	v_add_u32_e32 v25, v25, v24
	v_add_u32_e32 v26, v26, v25
	v_add_u32_e32 v27, v27, v26
	v_add_u32_e32 v28, v28, v27
	v_add_u32_e32 v29, v29, v28
	v_add_u32_e32 v30, v30, v29
	v_add_u32_e32 v31, v31, v30
	v_add_u32_e32 v32, v32, v31
	v_add_u32_e32 v33, v33, v32
	v_add_u32_e32 v34, v34, v33
	v_add_u32_e32 v35, v35, v34
	v_add_u32_e32 v36, v36, v35
	v_add_u32_e32 v37, v37, v36
	v_add_u32_e32 v38, v38, v37
	v_add_u32_e32 v39, v39, v38
	v_add_u32_e32 v40, v40, v39
	v_add_u32_e32 v41, v41, v40
	v_add_u32_e32 v42, v42, v41
	v_add_u32_e32 v43, v43, v42
	v_add_u32_e32 v44, v44, v43
	v_add_u32_e32 v45, v45, v44
	v_add_u32_e32 v46, v46, v45
	v_add_u32_e32 v47, v47, v46
	v_add_u32_e32 v48, v48, v47
	v_add_u32_e32 v49, v49, v48
	v_add_u32_e32 v50, v50, v49
	v_add_u32_e32 v51, v51, v50
	v_lshrrev_b32_e32 v10, 8, v51
	v_mov_b32_e32 v11, v8
	v_lshlrev_b32_e32 v12, 8, v11
	v_mov_b32_e32 v13, 0
	v_cmp_le_u32_e32 vcc, v20, v12
	v_addc_co_u32_e32 v13, vcc, 0, v13, vcc
	v_cmp_le_u32_e32 vcc, v21, v12
	v_addc_co_u32_e32 v13, vcc, 0, v13, vcc
	v_cmp_le_u32_e32 vcc, v22, v12
	v_addc_co_u32_e32 v13, vcc, 0, v13, vcc
	v_cmp_le_u32_e32 vcc, v23, v12
	v_addc_co_u32_e32 v13, vcc, 0, v13, vcc
	v_cmp_le_u32_e32 vcc, v24, v12
	v_addc_co_u32_e32 v13, vcc, 0, v13, vcc
	v_cmp_le_u32_e32 vcc, v25, v12
	v_addc_co_u32_e32 v13, vcc, 0, v13, vcc
	v_cmp_le_u32_e32 vcc, v26, v12
	v_addc_co_u32_e32 v13, vcc, 0, v13, vcc
	v_cmp_le_u32_e32 vcc, v27, v12
	v_addc_co_u32_e32 v13, vcc, 0, v13, vcc
	v_cmp_le_u32_e32 vcc, v28, v12
	v_addc_co_u32_e32 v13, vcc, 0, v13, vcc
	v_cmp_le_u32_e32 vcc, v29, v12
	v_addc_co_u32_e32 v13, vcc, 0, v13, vcc
	v_cmp_le_u32_e32 vcc, v30, v12
	v_addc_co_u32_e32 v13, vcc, 0, v13, vcc
	v_cmp_le_u32_e32 vcc, v31, v12
	v_addc_co_u32_e32 v13, vcc, 0, v13, vcc
	v_cmp_le_u32_e32 vcc, v32, v12
	v_addc_co_u32_e32 v13, vcc, 0, v13, vcc
	v_cmp_le_u32_e32 vcc, v33, v12
	v_addc_co_u32_e32 v13, vcc, 0, v13, vcc
	v_cmp_le_u32_e32 vcc, v34, v12
	v_addc_co_u32_e32 v13, vcc, 0, v13, vcc
	v_cmp_le_u32_e32 vcc, v35, v12
	v_addc_co_u32_e32 v13, vcc, 0, v13, vcc
	v_cmp_le_u32_e32 vcc, v36, v12
	v_addc_co_u32_e32 v13, vcc, 0, v13, vcc
	v_cmp_le_u32_e32 vcc, v37, v12
	v_addc_co_u32_e32 v13, vcc, 0, v13, vcc
	v_cmp_le_u32_e32 vcc, v38, v12
	v_addc_co_u32_e32 v13, vcc, 0, v13, vcc
	v_cmp_le_u32_e32 vcc, v39, v12
	v_addc_co_u32_e32 v13, vcc, 0, v13, vcc
	v_cmp_le_u32_e32 vcc, v40, v12
	v_addc_co_u32_e32 v13, vcc, 0, v13, vcc
	v_cmp_le_u32_e32 vcc, v41, v12
	v_addc_co_u32_e32 v13, vcc, 0, v13, vcc
	v_cmp_le_u32_e32 vcc, v42, v12
	v_addc_co_u32_e32 v13, vcc, 0, v13, vcc
	v_cmp_le_u32_e32 vcc, v43, v12
	v_addc_co_u32_e32 v13, vcc, 0, v13, vcc
	v_cmp_le_u32_e32 vcc, v44, v12
	v_addc_co_u32_e32 v13, vcc, 0, v13, vcc
	v_cmp_le_u32_e32 vcc, v45, v12
	v_addc_co_u32_e32 v13, vcc, 0, v13, vcc
	v_cmp_le_u32_e32 vcc, v46, v12
	v_addc_co_u32_e32 v13, vcc, 0, v13, vcc
	v_cmp_le_u32_e32 vcc, v47, v12
	v_addc_co_u32_e32 v13, vcc, 0, v13, vcc
	v_cmp_le_u32_e32 vcc, v48, v12
	v_addc_co_u32_e32 v13, vcc, 0, v13, vcc
	v_cmp_le_u32_e32 vcc, v49, v12
	v_addc_co_u32_e32 v13, vcc, 0, v13, vcc
	v_cmp_le_u32_e32 vcc, v50, v12
	v_addc_co_u32_e32 v13, vcc, 0, v13, vcc
	v_cmp_le_u32_e32 vcc, v51, v12
	v_addc_co_u32_e32 v13, vcc, 0, v13, vcc
	v_cmp_lt_u32_e32 vcc, v11, v10
	s_and_saveexec_b64 s[10:11], vcc
	v_lshlrev_b32_e32 v14, 1, v11
	v_add_u32_e32 v14, 0x201e0, v14
	ds_write_b16 v14, v13
	s_mov_b64 exec, s[10:11]
	v_add_u32_e32 v11, 0x200, v8
	v_lshlrev_b32_e32 v12, 8, v11
	v_mov_b32_e32 v13, 0
	v_cmp_le_u32_e32 vcc, v20, v12
	v_addc_co_u32_e32 v13, vcc, 0, v13, vcc
	v_cmp_le_u32_e32 vcc, v21, v12
	v_addc_co_u32_e32 v13, vcc, 0, v13, vcc
	v_cmp_le_u32_e32 vcc, v22, v12
	v_addc_co_u32_e32 v13, vcc, 0, v13, vcc
	v_cmp_le_u32_e32 vcc, v23, v12
	v_addc_co_u32_e32 v13, vcc, 0, v13, vcc
	v_cmp_le_u32_e32 vcc, v24, v12
	v_addc_co_u32_e32 v13, vcc, 0, v13, vcc
	v_cmp_le_u32_e32 vcc, v25, v12
	v_addc_co_u32_e32 v13, vcc, 0, v13, vcc
	v_cmp_le_u32_e32 vcc, v26, v12
	v_addc_co_u32_e32 v13, vcc, 0, v13, vcc
	v_cmp_le_u32_e32 vcc, v27, v12
	v_addc_co_u32_e32 v13, vcc, 0, v13, vcc
	v_cmp_le_u32_e32 vcc, v28, v12
	v_addc_co_u32_e32 v13, vcc, 0, v13, vcc
	v_cmp_le_u32_e32 vcc, v29, v12
	v_addc_co_u32_e32 v13, vcc, 0, v13, vcc
	v_cmp_le_u32_e32 vcc, v30, v12
	v_addc_co_u32_e32 v13, vcc, 0, v13, vcc
	v_cmp_le_u32_e32 vcc, v31, v12
	v_addc_co_u32_e32 v13, vcc, 0, v13, vcc
	v_cmp_le_u32_e32 vcc, v32, v12
	v_addc_co_u32_e32 v13, vcc, 0, v13, vcc
	v_cmp_le_u32_e32 vcc, v33, v12
	v_addc_co_u32_e32 v13, vcc, 0, v13, vcc
	v_cmp_le_u32_e32 vcc, v34, v12
	v_addc_co_u32_e32 v13, vcc, 0, v13, vcc
	v_cmp_le_u32_e32 vcc, v35, v12
	v_addc_co_u32_e32 v13, vcc, 0, v13, vcc
	v_cmp_le_u32_e32 vcc, v36, v12
	v_addc_co_u32_e32 v13, vcc, 0, v13, vcc
	v_cmp_le_u32_e32 vcc, v37, v12
	v_addc_co_u32_e32 v13, vcc, 0, v13, vcc
	v_cmp_le_u32_e32 vcc, v38, v12
	v_addc_co_u32_e32 v13, vcc, 0, v13, vcc
	v_cmp_le_u32_e32 vcc, v39, v12
	v_addc_co_u32_e32 v13, vcc, 0, v13, vcc
	v_cmp_le_u32_e32 vcc, v40, v12
	v_addc_co_u32_e32 v13, vcc, 0, v13, vcc
	v_cmp_le_u32_e32 vcc, v41, v12
	v_addc_co_u32_e32 v13, vcc, 0, v13, vcc
	v_cmp_le_u32_e32 vcc, v42, v12
	v_addc_co_u32_e32 v13, vcc, 0, v13, vcc
	v_cmp_le_u32_e32 vcc, v43, v12
	v_addc_co_u32_e32 v13, vcc, 0, v13, vcc
	v_cmp_le_u32_e32 vcc, v44, v12
	v_addc_co_u32_e32 v13, vcc, 0, v13, vcc
	v_cmp_le_u32_e32 vcc, v45, v12
	v_addc_co_u32_e32 v13, vcc, 0, v13, vcc
	v_cmp_le_u32_e32 vcc, v46, v12
	v_addc_co_u32_e32 v13, vcc, 0, v13, vcc
	v_cmp_le_u32_e32 vcc, v47, v12
	v_addc_co_u32_e32 v13, vcc, 0, v13, vcc
	v_cmp_le_u32_e32 vcc, v48, v12
	v_addc_co_u32_e32 v13, vcc, 0, v13, vcc
	v_cmp_le_u32_e32 vcc, v49, v12
	v_addc_co_u32_e32 v13, vcc, 0, v13, vcc
	v_cmp_le_u32_e32 vcc, v50, v12
	v_addc_co_u32_e32 v13, vcc, 0, v13, vcc
	v_cmp_le_u32_e32 vcc, v51, v12
	v_addc_co_u32_e32 v13, vcc, 0, v13, vcc
	v_cmp_lt_u32_e32 vcc, v11, v10
	s_and_saveexec_b64 s[10:11], vcc
	v_lshlrev_b32_e32 v14, 1, v11
	v_add_u32_e32 v14, 0x201e0, v14
	ds_write_b16 v14, v13
	s_mov_b64 exec, s[10:11]
	v_add_u32_e32 v11, 0x400, v8
	v_lshlrev_b32_e32 v12, 8, v11
	v_mov_b32_e32 v13, 0
	v_cmp_le_u32_e32 vcc, v20, v12
	v_addc_co_u32_e32 v13, vcc, 0, v13, vcc
	v_cmp_le_u32_e32 vcc, v21, v12
	v_addc_co_u32_e32 v13, vcc, 0, v13, vcc
	v_cmp_le_u32_e32 vcc, v22, v12
	v_addc_co_u32_e32 v13, vcc, 0, v13, vcc
	v_cmp_le_u32_e32 vcc, v23, v12
	v_addc_co_u32_e32 v13, vcc, 0, v13, vcc
	v_cmp_le_u32_e32 vcc, v24, v12
	v_addc_co_u32_e32 v13, vcc, 0, v13, vcc
	v_cmp_le_u32_e32 vcc, v25, v12
	v_addc_co_u32_e32 v13, vcc, 0, v13, vcc
	v_cmp_le_u32_e32 vcc, v26, v12
	v_addc_co_u32_e32 v13, vcc, 0, v13, vcc
	v_cmp_le_u32_e32 vcc, v27, v12
	v_addc_co_u32_e32 v13, vcc, 0, v13, vcc
	v_cmp_le_u32_e32 vcc, v28, v12
	v_addc_co_u32_e32 v13, vcc, 0, v13, vcc
	v_cmp_le_u32_e32 vcc, v29, v12
	v_addc_co_u32_e32 v13, vcc, 0, v13, vcc
	v_cmp_le_u32_e32 vcc, v30, v12
	v_addc_co_u32_e32 v13, vcc, 0, v13, vcc
	v_cmp_le_u32_e32 vcc, v31, v12
	v_addc_co_u32_e32 v13, vcc, 0, v13, vcc
	v_cmp_le_u32_e32 vcc, v32, v12
	v_addc_co_u32_e32 v13, vcc, 0, v13, vcc
	v_cmp_le_u32_e32 vcc, v33, v12
	v_addc_co_u32_e32 v13, vcc, 0, v13, vcc
	v_cmp_le_u32_e32 vcc, v34, v12
	v_addc_co_u32_e32 v13, vcc, 0, v13, vcc
	v_cmp_le_u32_e32 vcc, v35, v12
	v_addc_co_u32_e32 v13, vcc, 0, v13, vcc
	v_cmp_le_u32_e32 vcc, v36, v12
	v_addc_co_u32_e32 v13, vcc, 0, v13, vcc
	v_cmp_le_u32_e32 vcc, v37, v12
	v_addc_co_u32_e32 v13, vcc, 0, v13, vcc
	v_cmp_le_u32_e32 vcc, v38, v12
	v_addc_co_u32_e32 v13, vcc, 0, v13, vcc
	v_cmp_le_u32_e32 vcc, v39, v12
	v_addc_co_u32_e32 v13, vcc, 0, v13, vcc
	v_cmp_le_u32_e32 vcc, v40, v12
	v_addc_co_u32_e32 v13, vcc, 0, v13, vcc
	v_cmp_le_u32_e32 vcc, v41, v12
	v_addc_co_u32_e32 v13, vcc, 0, v13, vcc
	v_cmp_le_u32_e32 vcc, v42, v12
	v_addc_co_u32_e32 v13, vcc, 0, v13, vcc
	v_cmp_le_u32_e32 vcc, v43, v12
	v_addc_co_u32_e32 v13, vcc, 0, v13, vcc
	v_cmp_le_u32_e32 vcc, v44, v12
	v_addc_co_u32_e32 v13, vcc, 0, v13, vcc
	v_cmp_le_u32_e32 vcc, v45, v12
	v_addc_co_u32_e32 v13, vcc, 0, v13, vcc
	v_cmp_le_u32_e32 vcc, v46, v12
	v_addc_co_u32_e32 v13, vcc, 0, v13, vcc
	v_cmp_le_u32_e32 vcc, v47, v12
	v_addc_co_u32_e32 v13, vcc, 0, v13, vcc
	v_cmp_le_u32_e32 vcc, v48, v12
	v_addc_co_u32_e32 v13, vcc, 0, v13, vcc
	v_cmp_le_u32_e32 vcc, v49, v12
	v_addc_co_u32_e32 v13, vcc, 0, v13, vcc
	v_cmp_le_u32_e32 vcc, v50, v12
	v_addc_co_u32_e32 v13, vcc, 0, v13, vcc
	v_cmp_le_u32_e32 vcc, v51, v12
	v_addc_co_u32_e32 v13, vcc, 0, v13, vcc
	v_cmp_lt_u32_e32 vcc, v11, v10
	s_and_saveexec_b64 s[10:11], vcc
	v_lshlrev_b32_e32 v14, 1, v11
	v_add_u32_e32 v14, 0x201e0, v14
	ds_write_b16 v14, v13
	s_mov_b64 exec, s[10:11]
	s_cmp_lg_u32 s86, 0
	s_cbranch_scc1 .Ltab_done
	s_mov_b64 exec, 1
	v_mov_b32_e32 v14, 0x200c0
	v_mov_b32_e32 v15, 0
	v_readlane_b32 s11, v253, 9
	ds_write_b32 v14, v15
	ds_write_b32 v14, v20 offset:4
	ds_write_b32 v14, v21 offset:8
	ds_write_b32 v14, v22 offset:12
	ds_write_b32 v14, v23 offset:16
	ds_write_b32 v14, v24 offset:20
	ds_write_b32 v14, v25 offset:24
	ds_write_b32 v14, v26 offset:28
	ds_write_b32 v14, v27 offset:32
	ds_write_b32 v14, v28 offset:36
	ds_write_b32 v14, v29 offset:40
	ds_write_b32 v14, v30 offset:44
	ds_write_b32 v14, v31 offset:48
	ds_write_b32 v14, v32 offset:52
	ds_write_b32 v14, v33 offset:56
	ds_write_b32 v14, v34 offset:60
	ds_write_b32 v14, v35 offset:64
	ds_write_b32 v14, v36 offset:68
	ds_write_b32 v14, v37 offset:72
	ds_write_b32 v14, v38 offset:76
	ds_write_b32 v14, v39 offset:80
	ds_write_b32 v14, v40 offset:84
	ds_write_b32 v14, v41 offset:88
	ds_write_b32 v14, v42 offset:92
	ds_write_b32 v14, v43 offset:96
	ds_write_b32 v14, v44 offset:100
	ds_write_b32 v14, v45 offset:104
	ds_write_b32 v14, v46 offset:108
	ds_write_b32 v14, v47 offset:112
	ds_write_b32 v14, v48 offset:116
	ds_write_b32 v14, v49 offset:120
	ds_write_b32 v14, v50 offset:124
	ds_write_b32 v14, v51 offset:128
	v_mov_b32_e32 v15, s11
	ds_write_b32 v15, v10
	s_mov_b64 exec, -1
.Ltab_done:
	s_mov_b64 s[0:1], exec
.LBB0_1112:
	s_or_b64 exec, exec, s[0:1]
	s_mov_b32 s10, s86
	s_waitcnt lgkmcnt(0)
	s_barrier
	v_lshl_add_u32 v0, s86, 6, v213
	s_add_u32 s26, s6, 0x2b500000
	s_addc_u32 s27, s7, 0
	v_readlane_b32 s0, v252, 6
	v_readlane_b32 s1, v252, 7
	s_nop 0
	s_andn2_b64 vcc, exec, s[0:1]
	s_cbranch_vccnz .Lgat_nopad
	v_readlane_b32 s0, v252, 9
	v_readlane_b32 s1, v252, 10
	s_nop 0
	v_mov_b32_e32 v2, s0
	ds_read2_b32 v[2:3], v2 offset1:1
	v_mov_b32_e32 v4, s1
	ds_read_b32 v4, v4
	v_mov_b32_e32 v5, 0x10800
	s_waitcnt lgkmcnt(0)
	v_add3_u32 v2, v2, v4, v0
	s_mov_b64 s[28:29], exec
